# chunk phase: the g/beta loads of the decay scan issued with the item's other up-front loads instead of after the LDS tile stores (one less exposed round trip before the item barrier)
# baseline (speedup 1.0000x reference)
.LBB0_411:
	s_add_i32 s2, s26, s50
	s_ashr_i32 s2, s2, 1
	s_mul_hi_i32 s4, s2, 0x78787879
	s_ashr_i32 s6, s4, 5
	s_lshr_b32 s7, s4, 31
	s_add_i32 s6, s6, s7
	s_mul_i32 s12, s6, 0x44
	s_ashr_i32 s4, s4, 7
	s_sub_i32 s2, s2, s12
	s_and_b32 s13, s6, 3
	s_add_i32 s25, s4, s7
	s_cmp_gt_i32 s2, 3
	s_cselect_b32 s4, 0x47, 3
	s_sub_i32 s4, s4, s2
	s_and_b64 s[6:7], s[38:39], exec
	s_cselect_b32 s2, s2, s4
	s_mul_i32 s4, s25, 0x110
	s_add_i32 s4, s4, s51
	s_mul_i32 s6, s13, 0x44
	v_mov_b32_e32 v67, v64
	s_add_i32 s4, s4, s6
	s_add_i32 s6, s4, s2
	v_and_b32_e32 v65, 0x7f, v67
	s_ashr_i32 s7, s6, 31
	s_lshl_b32 s12, s2, 6
	v_or_b32_e32 v66, 0x80, v65
	s_cmp_lt_i32 s2, 4
	s_movk_i32 s2, 0x11ff
	v_bfe_u32 v2, v67, 4, 3
	v_lshrrev_b32_e32 v4, 4, v66
	v_and_b32_e32 v0, 8, v67
	s_cselect_b32 s2, 0xff, s2
	v_or_b32_e32 v18, s12, v2
	v_or_b32_e32 v4, s12, v4
	v_cmp_eq_u32_e32 vcc, 0, v0
	v_mov_b32_e32 v0, 0x4400000
	v_sub_u32_e32 v2, s2, v18
	v_sub_u32_e32 v5, s2, v4
	v_cndmask_b32_e32 v112, v0, v203, vcc
	v_cndmask_b32_e64 v2, v2, v18, s[38:39]
	v_cndmask_b32_e64 v4, v5, v4, s[38:39]
	v_lshl_add_u64 v[0:1], s[18:19], 0, v[112:113]
	s_lshl_b32 s4, s13, 7
	v_lshlrev_b32_e32 v68, 4, v67
	v_ashrrev_i32_e32 v3, 31, v2
	v_ashrrev_i32_e32 v5, 31, v4
	v_lshl_add_u64 v[0:1], v[0:1], 0, s[4:5]
	v_and_b32_e32 v112, 0x70, v68
	v_mad_i64_i32 v[2:3], s[14:15], s25, v204, v[2:3]
	v_mad_i64_i32 v[4:5], s[14:15], s25, v204, v[4:5]
	v_lshl_add_u64 v[0:1], v[0:1], 0, v[112:113]
	v_lshlrev_b64 v[2:3], 9, v[2:3]
	v_lshlrev_b64 v[4:5], 9, v[4:5]
	v_lshl_add_u64 v[2:3], v[0:1], 0, v[2:3]
	v_lshl_add_u64 v[8:9], v[0:1], 0, v[4:5]
	s_waitcnt vmcnt(0)
	s_barrier
	global_load_dwordx4 v[4:7], v[2:3], off
	s_nop 0
	global_load_dwordx4 v[8:11], v[8:9], off
	v_or_b32_e32 v2, 16, v18
	v_or_b32_e32 v12, 24, v18
	v_sub_u32_e32 v3, s2, v2
	v_sub_u32_e32 v13, s2, v12
	v_cndmask_b32_e64 v2, v3, v2, s[38:39]
	v_cndmask_b32_e64 v12, v13, v12, s[38:39]
	v_ashrrev_i32_e32 v3, 31, v2
	v_ashrrev_i32_e32 v13, 31, v12
	v_mad_i64_i32 v[2:3], s[14:15], s25, v204, v[2:3]
	v_mad_i64_i32 v[12:13], s[14:15], s25, v204, v[12:13]
	v_lshlrev_b64 v[2:3], 9, v[2:3]
	v_lshlrev_b64 v[12:13], 9, v[12:13]
	v_lshl_add_u64 v[2:3], v[0:1], 0, v[2:3]
	v_lshl_add_u64 v[16:17], v[0:1], 0, v[12:13]
	global_load_dwordx4 v[12:15], v[2:3], off
	global_load_dwordx4 v[44:47], v[16:17], off
	v_or_b32_e32 v2, 32, v18
	v_or_b32_e32 v16, 40, v18
	v_sub_u32_e32 v3, s2, v2
	v_sub_u32_e32 v17, s2, v16
	v_cndmask_b32_e64 v2, v3, v2, s[38:39]
	v_cndmask_b32_e64 v16, v17, v16, s[38:39]
	v_ashrrev_i32_e32 v3, 31, v2
	v_ashrrev_i32_e32 v17, 31, v16
	v_mad_i64_i32 v[2:3], s[14:15], s25, v204, v[2:3]
	v_mad_i64_i32 v[16:17], s[14:15], s25, v204, v[16:17]
	v_lshlrev_b64 v[2:3], 9, v[2:3]
	v_lshlrev_b64 v[16:17], 9, v[16:17]
	v_lshl_add_u64 v[2:3], v[0:1], 0, v[2:3]
	v_lshl_add_u64 v[16:17], v[0:1], 0, v[16:17]
	global_load_dwordx4 v[48:51], v[2:3], off
	global_load_dwordx4 v[52:55], v[16:17], off
	v_or_b32_e32 v2, 48, v18
	v_or_b32_e32 v16, 56, v18
	v_sub_u32_e32 v3, s2, v2
	v_sub_u32_e32 v17, s2, v16
	v_cndmask_b32_e64 v2, v3, v2, s[38:39]
	v_cndmask_b32_e64 v16, v17, v16, s[38:39]
	v_ashrrev_i32_e32 v3, 31, v2
	v_ashrrev_i32_e32 v17, 31, v16
	v_mad_i64_i32 v[2:3], s[14:15], s25, v204, v[2:3]
	v_mad_i64_i32 v[16:17], s[14:15], s25, v204, v[16:17]
	v_and_b32_e32 v73, 31, v67
	v_lshlrev_b64 v[2:3], 9, v[2:3]
	v_lshlrev_b64 v[16:17], 9, v[16:17]
	v_lshl_add_u64 v[2:3], v[0:1], 0, v[2:3]
	v_lshl_add_u64 v[0:1], v[0:1], 0, v[16:17]
	v_or_b32_e32 v20, s12, v73
	global_load_dwordx4 v[56:59], v[2:3], off
	global_load_dwordx4 v[60:63], v[0:1], off
	v_sub_u32_e32 v0, s2, v20
	v_cndmask_b32_e64 v0, v0, v20, s[38:39]
	v_bfe_u32 v75, v67, 5, 1
	s_add_u32 s70, s18, s4
	v_ashrrev_i32_e32 v1, 31, v0
	s_addc_u32 s71, s19, 0
	v_lshlrev_b32_e32 v112, 4, v75
	v_mad_i64_i32 v[0:1], s[14:15], s25, v204, v[0:1]
	v_lshl_add_u64 v[16:17], s[70:71], 0, v[112:113]
	v_lshlrev_b64 v[0:1], 9, v[0:1]
	v_lshl_add_u64 v[18:19], v[16:17], 0, v[0:1]
	global_load_dwordx4 v[0:3], v[18:19], off
	global_load_dwordx4 v[40:43], v[18:19], off offset:32
	global_load_dwordx4 v[36:39], v[18:19], off offset:64
	global_load_dwordx4 v[32:35], v[18:19], off offset:96
	v_or_b32_e32 v18, 32, v20
	v_sub_u32_e32 v19, s2, v18
	v_cndmask_b32_e64 v18, v19, v18, s[38:39]
	v_ashrrev_i32_e32 v19, 31, v18
	v_mad_i64_i32 v[18:19], s[14:15], s25, v204, v[18:19]
	v_lshlrev_b64 v[18:19], 9, v[18:19]
	v_lshl_add_u64 v[16:17], v[16:17], 0, v[18:19]
	global_load_dwordx4 v[24:27], v[16:17], off
	global_load_dwordx4 v[28:31], v[16:17], off offset:32
	global_load_dwordx4 v[20:23], v[16:17], off offset:64
	s_nop 0
	global_load_dwordx4 v[16:19], v[16:17], off offset:96
	v_and_b32_e32 v69, 0x700, v68
	v_and_b32_e32 v68, 0xf0, v68
	s_mul_hi_i32 s65, s25, 0x1100
	s_mul_i32 s64, s25, 0x1100
	v_and_b32_e32 v242, 63, v67
	v_or_b32_e32 v244, s12, v242
	v_sub_u32_e32 v245, s2, v244
	v_cndmask_b32_e64 v244, v245, v244, s[38:39]
	v_ashrrev_i32_e32 v245, 31, v244
	v_lshl_add_u64 v[244:245], s[64:65], 0, v[244:245]
	v_lshlrev_b64 v[244:245], 6, v[244:245]
	v_lshl_add_u64 v[244:245], s[48:49], 0, v[244:245]
	s_lshl_b32 s98, s13, 2
	s_mov_b32 s99, 0
	v_lshl_add_u64 v[244:245], v[244:245], 0, s[98:99]
	global_load_dword v240, v[244:245], off
	global_load_dword v241, v[244:245], off offset:32
	v_add3_u32 v68, s27, v69, v68
	s_andn2_b64 vcc, exec, s[42:43]
	s_waitcnt vmcnt(17)
	ds_write_b128 v68, v[4:7] offset:17408
	s_waitcnt vmcnt(16)
	ds_write_b128 v68, v[8:11] offset:19456
	s_waitcnt vmcnt(15)
	ds_write_b128 v68, v[12:15] offset:21504
	s_waitcnt vmcnt(14)
	ds_write_b128 v68, v[44:47] offset:23552
	s_waitcnt vmcnt(13)
	ds_write_b128 v68, v[48:51] offset:25600
	s_waitcnt vmcnt(12)
	ds_write_b128 v68, v[52:55] offset:27648
	s_waitcnt vmcnt(11)
	ds_write_b128 v68, v[56:59] offset:29696
	s_waitcnt vmcnt(10)
	ds_write_b128 v68, v[60:63] offset:31744
	s_cbranch_vccnz .LBB0_415
	v_and_b32_e32 v6, 63, v67
	s_waitcnt vmcnt(0)
	v_mov_b32_e32 v7, v240
	v_mov_b32_e32 v4, v241
	v_lshlrev_b32_e32 v5, 2, v67
	v_add_u32_e32 v8, 0xfc, v5
	v_and_b32_e32 v8, 0xfc, v8
	v_cmp_eq_u32_e32 vcc, 0, v6
	v_cmp_gt_u32_e64 s[40:41], 2, v6
	s_movk_i32 s4, 0x80
	s_waitcnt vmcnt(1)
	ds_bpermute_b32 v8, v8, v7
	s_waitcnt lgkmcnt(0)
	v_add_f32_e32 v8, v7, v8
	v_cndmask_b32_e32 v7, v8, v7, vcc
	v_add_u32_e32 v8, 0xf8, v5
	v_and_b32_e32 v8, 0xfc, v8
	ds_bpermute_b32 v8, v8, v7
	s_waitcnt lgkmcnt(0)
	v_add_f32_e32 v8, v7, v8
	v_cndmask_b32_e64 v7, v8, v7, s[40:41]
	v_add_u32_e32 v8, 0xf0, v5
	v_and_b32_e32 v8, 0xfc, v8
	ds_bpermute_b32 v8, v8, v7
	v_cmp_gt_u32_e64 s[40:41], 4, v6
	s_waitcnt lgkmcnt(0)
	v_add_f32_e32 v8, v7, v8
	v_cndmask_b32_e64 v7, v8, v7, s[40:41]
	v_add_u32_e32 v8, 0xe0, v5
	v_and_b32_e32 v8, 0xfc, v8
	ds_bpermute_b32 v8, v8, v7
	v_cmp_gt_u32_e64 s[40:41], 8, v6
	s_waitcnt lgkmcnt(0)
	v_add_f32_e32 v8, v7, v8
	v_cndmask_b32_e64 v7, v8, v7, s[40:41]
	v_add_u32_e32 v8, 0xc0, v5
	v_and_b32_e32 v8, 0xfc, v8
	ds_bpermute_b32 v8, v8, v7
	v_cmp_gt_u32_e64 s[40:41], 16, v6
	s_waitcnt lgkmcnt(0)
	v_add_f32_e32 v8, v7, v8
	v_cndmask_b32_e64 v7, v8, v7, s[40:41]
	v_bfrev_b32_e32 v8, 0.5
	v_bitop3_b32 v5, v5, s4, v8 bitop3:0x6c
	ds_bpermute_b32 v5, v5, v7
	v_cmp_gt_u32_e64 s[40:41], 32, v6
	v_lshl_add_u32 v6, v6, 2, s27
	s_waitcnt lgkmcnt(0)
	v_add_f32_e32 v5, v7, v5
	v_cndmask_b32_e64 v5, v5, v7, s[40:41]
	s_waitcnt vmcnt(0)
	ds_write2st64_b32 v6, v5, v4 offset0:64 offset1:65
	v_readlane_b32 s4, v5, 63
	v_mul_f32_e32 v4, 0x3fb8aa3b, v5
	v_exp_f32_e32 v4, v4
	v_sub_f32_e32 v5, s4, v5
	v_mul_f32_e32 v5, 0x3fb8aa3b, v5
	v_exp_f32_e32 v5, v5
	ds_write2st64_b32 v6, v4, v5 offset0:66 offset1:67
	s_and_saveexec_b64 s[40:41], vcc
	s_cbranch_execz .LBB0_414
	v_mul_f32_e32 v4, s4, v248
	v_exp_f32_e32 v4, v4
	s_lshl_b64 s[14:15], s[6:7], 2
	s_add_u32 s14, s67, s14
	s_addc_u32 s15, s0, s15
	global_store_dword v113, v4, s[14:15]
